# v29 + GLA scan step waits for its four helper flags with one 16-byte LDS read instead of four serial reads
# speedup vs baseline: 1.0052x; 1.0052x over previous
.Lsc_poll:
	v_mov_b32_e32 v66, s11
	ds_read_b128 v[66:69], v66
	s_waitcnt lgkmcnt(0)
	v_min_u32_e32 v66, v66, v67
	v_min3_u32 v66, v66, v68, v69
	v_cmp_lt_u32_e32 vcc, s10, v66
	s_cbranch_vccnz .LBB0_569
	s_add_i32 s18, s18, -1
	s_cmp_eq_u32 s18, 0
	s_cbranch_scc1 .LBB0_569
	s_sleep 1
	s_branch .Lsc_poll
